# agg gather dequant: messages stored as u8=q+128; one v_perm makes two exact f16 (1024+u) values, v_fma_mix_f32 accumulates in f32, 1152*sum(scale) removed once per node (13 VALU per edge instead of 16
# baseline (speedup 1.0000x reference)
_Z7agg_ln1PKDF16_S0_S0_PKiS2_S2_PKfS4_S4_PDF16_S4_S4_S5_S5_:
	s_cmpk_gt_u32 s2, 0xff
	s_mov_b64 s[4:5], -1
	s_cbranch_scc0 .LBB1_28
	v_lshl_or_b32 v1, s2, 8, v0
	v_add_u32_e32 v1, 0xffff0000, v1
	s_mov_b32 s3, 0x9c400
	v_cmp_gt_u32_e32 vcc, s3, v1
	s_and_saveexec_b64 s[18:19], vcc
	s_cbranch_execz .LBB1_27
	s_load_dwordx2 s[4:5], s[0:1], 0x20
	s_load_dwordx2 s[6:7], s[0:1], 0x18
	s_load_dwordx2 s[32:33], s[0:1], 0x8
	v_lshrrev_b32_e32 v1, 6, v1
	v_lshlrev_b32_e32 v2, 4, v1
	v_and_b32_e32 v24, 63, v0
	v_lshlrev_b32_e32 v8, 3, v24
	v_lshlrev_b32_e32 v21, 10, v1
	v_lshl_add_u32 v21, v24, 4, v21
	s_waitcnt lgkmcnt(0)
	global_load_dwordx4 v[28:31], v2, s[6:7]
	global_load_dwordx4 v[2:5], v2, s[4:5]
	global_load_dwordx4 v[60:63], v21, s[32:33] nt
	s_waitcnt vmcnt(0)
	v_add_u32_e32 v26, v3, v2
	v_add_u32_e32 v3, v26, v4
	v_add_u32_e32 v25, v3, v5
	v_cmp_gt_i32_e32 vcc, 1, v25
	s_and_saveexec_b64 s[4:5], vcc
	s_xor_b64 s[4:5], exec, s[4:5]
	v_mov_b32_e32 v9, 0
	s_or_saveexec_b64 s[22:23], s[4:5]
	s_load_dwordx2 s[20:21], s[0:1], 0x48
	v_mov_b32_e32 v11, 0
	v_mov_b64_e32 v[18:19], 0
	v_mov_b32_e32 v27, 0
	v_mov_b32_e32 v10, v11
	v_mov_b32_e32 v13, v11
	v_mov_b32_e32 v12, v11
	v_mov_b32_e32 v15, v11
	v_mov_b32_e32 v14, v11
	v_mov_b32_e32 v17, v11
	v_mov_b32_e32 v16, v11
	s_xor_b64 exec, exec, s[22:23]
	s_cbranch_execz .LBB1_26
	s_load_dwordx2 s[24:25], s[0:1], 0x28
	s_load_dwordx2 s[26:27], s[0:1], 0x0
	v_readfirstlane_b32 s2, v25
	v_readfirstlane_b32 s4, v2
	v_readfirstlane_b32 s5, v26
	v_readfirstlane_b32 s6, v3
	v_readfirstlane_b32 s8, v28
	v_readfirstlane_b32 s9, v29
	v_readfirstlane_b32 s10, v30
	v_readfirstlane_b32 s11, v31
	v_lshrrev_b32_e32 v20, 3, v24
	v_lshlrev_b32_e32 v20, 2, v20
	v_mov_b32_e32 v26, 0x64646464
	s_mov_b32 s56, 0x00050004
	s_mov_b32 s57, 0x00070006
	v_mov_b32_e32 v9, 0
	v_mov_b32_e32 v10, 0
	v_mov_b32_e32 v11, 0
	v_mov_b32_e32 v12, 0
	v_mov_b32_e32 v13, 0
	v_mov_b32_e32 v14, 0
	v_mov_b32_e32 v15, 0
	v_mov_b32_e32 v16, 0
	v_mov_b32_e32 v17, 0
	s_sub_u32 s9, s9, s4
	s_sub_u32 s10, s10, s5
	s_sub_u32 s11, s11, s6
	s_mov_b64 s[12:13], 0
	s_mov_b32 s3, 0
	s_sub_u32 s7, s2, 1
	s_waitcnt lgkmcnt(0)

.Lagg_ac7:
	s_waitcnt vmcnt(14)
	v_perm_b32 v2, v54, v26, s56
	v_perm_b32 v3, v54, v26, s57
	v_perm_b32 v22, v55, v26, s56
	v_perm_b32 v23, v55, v26, s57
	v_fma_mix_f32 v16, v2, v39, v16 op_sel_hi:[1,0,0]
	v_fma_mix_f32 v17, v2, v39, v17 op_sel:[1,0,0] op_sel_hi:[1,0,0]
	v_fma_mix_f32 v14, v3, v39, v14 op_sel_hi:[1,0,0]
	v_fma_mix_f32 v15, v3, v39, v15 op_sel:[1,0,0] op_sel_hi:[1,0,0]
	v_fma_mix_f32 v12, v22, v39, v12 op_sel_hi:[1,0,0]
	v_fma_mix_f32 v13, v22, v39, v13 op_sel:[1,0,0] op_sel_hi:[1,0,0]
	v_fma_mix_f32 v10, v23, v39, v10 op_sel_hi:[1,0,0]
	v_fma_mix_f32 v11, v23, v39, v11 op_sel:[1,0,0] op_sel_hi:[1,0,0]
	v_add_f32_e32 v27, v27, v39
.Lagg_ac6:
	s_waitcnt vmcnt(12)
	v_perm_b32 v2, v52, v26, s56
	v_perm_b32 v3, v52, v26, s57
	v_perm_b32 v22, v53, v26, s56
	v_perm_b32 v23, v53, v26, s57
	v_fma_mix_f32 v16, v2, v38, v16 op_sel_hi:[1,0,0]
	v_fma_mix_f32 v17, v2, v38, v17 op_sel:[1,0,0] op_sel_hi:[1,0,0]
	v_fma_mix_f32 v14, v3, v38, v14 op_sel_hi:[1,0,0]
	v_fma_mix_f32 v15, v3, v38, v15 op_sel:[1,0,0] op_sel_hi:[1,0,0]
	v_fma_mix_f32 v12, v22, v38, v12 op_sel_hi:[1,0,0]
	v_fma_mix_f32 v13, v22, v38, v13 op_sel:[1,0,0] op_sel_hi:[1,0,0]
	v_fma_mix_f32 v10, v23, v38, v10 op_sel_hi:[1,0,0]
	v_fma_mix_f32 v11, v23, v38, v11 op_sel:[1,0,0] op_sel_hi:[1,0,0]
	v_add_f32_e32 v27, v27, v38
.Lagg_ac5:
	s_waitcnt vmcnt(10)
	v_perm_b32 v2, v50, v26, s56
	v_perm_b32 v3, v50, v26, s57
	v_perm_b32 v22, v51, v26, s56
	v_perm_b32 v23, v51, v26, s57
	v_fma_mix_f32 v16, v2, v37, v16 op_sel_hi:[1,0,0]
	v_fma_mix_f32 v17, v2, v37, v17 op_sel:[1,0,0] op_sel_hi:[1,0,0]
	v_fma_mix_f32 v14, v3, v37, v14 op_sel_hi:[1,0,0]
	v_fma_mix_f32 v15, v3, v37, v15 op_sel:[1,0,0] op_sel_hi:[1,0,0]
	v_fma_mix_f32 v12, v22, v37, v12 op_sel_hi:[1,0,0]
	v_fma_mix_f32 v13, v22, v37, v13 op_sel:[1,0,0] op_sel_hi:[1,0,0]
	v_fma_mix_f32 v10, v23, v37, v10 op_sel_hi:[1,0,0]
	v_fma_mix_f32 v11, v23, v37, v11 op_sel:[1,0,0] op_sel_hi:[1,0,0]
	v_add_f32_e32 v27, v27, v37
.Lagg_ac4:
	s_waitcnt vmcnt(8)
	v_perm_b32 v2, v48, v26, s56
	v_perm_b32 v3, v48, v26, s57
	v_perm_b32 v22, v49, v26, s56
	v_perm_b32 v23, v49, v26, s57
	v_fma_mix_f32 v16, v2, v36, v16 op_sel_hi:[1,0,0]
	v_fma_mix_f32 v17, v2, v36, v17 op_sel:[1,0,0] op_sel_hi:[1,0,0]
	v_fma_mix_f32 v14, v3, v36, v14 op_sel_hi:[1,0,0]
	v_fma_mix_f32 v15, v3, v36, v15 op_sel:[1,0,0] op_sel_hi:[1,0,0]
	v_fma_mix_f32 v12, v22, v36, v12 op_sel_hi:[1,0,0]
	v_fma_mix_f32 v13, v22, v36, v13 op_sel:[1,0,0] op_sel_hi:[1,0,0]
	v_fma_mix_f32 v10, v23, v36, v10 op_sel_hi:[1,0,0]
	v_fma_mix_f32 v11, v23, v36, v11 op_sel:[1,0,0] op_sel_hi:[1,0,0]
	v_add_f32_e32 v27, v27, v36
.Lagg_ac3:
	s_waitcnt vmcnt(6)
	v_perm_b32 v2, v46, v26, s56
	v_perm_b32 v3, v46, v26, s57
	v_perm_b32 v22, v47, v26, s56
	v_perm_b32 v23, v47, v26, s57
	v_fma_mix_f32 v16, v2, v35, v16 op_sel_hi:[1,0,0]
	v_fma_mix_f32 v17, v2, v35, v17 op_sel:[1,0,0] op_sel_hi:[1,0,0]
	v_fma_mix_f32 v14, v3, v35, v14 op_sel_hi:[1,0,0]
	v_fma_mix_f32 v15, v3, v35, v15 op_sel:[1,0,0] op_sel_hi:[1,0,0]
	v_fma_mix_f32 v12, v22, v35, v12 op_sel_hi:[1,0,0]
	v_fma_mix_f32 v13, v22, v35, v13 op_sel:[1,0,0] op_sel_hi:[1,0,0]
	v_fma_mix_f32 v10, v23, v35, v10 op_sel_hi:[1,0,0]
	v_fma_mix_f32 v11, v23, v35, v11 op_sel:[1,0,0] op_sel_hi:[1,0,0]
	v_add_f32_e32 v27, v27, v35
.Lagg_ac2:
	s_waitcnt vmcnt(4)
	v_perm_b32 v2, v44, v26, s56
	v_perm_b32 v3, v44, v26, s57
	v_perm_b32 v22, v45, v26, s56
	v_perm_b32 v23, v45, v26, s57
	v_fma_mix_f32 v16, v2, v34, v16 op_sel_hi:[1,0,0]
	v_fma_mix_f32 v17, v2, v34, v17 op_sel:[1,0,0] op_sel_hi:[1,0,0]
	v_fma_mix_f32 v14, v3, v34, v14 op_sel_hi:[1,0,0]
	v_fma_mix_f32 v15, v3, v34, v15 op_sel:[1,0,0] op_sel_hi:[1,0,0]
	v_fma_mix_f32 v12, v22, v34, v12 op_sel_hi:[1,0,0]
	v_fma_mix_f32 v13, v22, v34, v13 op_sel:[1,0,0] op_sel_hi:[1,0,0]
	v_fma_mix_f32 v10, v23, v34, v10 op_sel_hi:[1,0,0]
	v_fma_mix_f32 v11, v23, v34, v11 op_sel:[1,0,0] op_sel_hi:[1,0,0]
	v_add_f32_e32 v27, v27, v34
.Lagg_ac1:
	s_waitcnt vmcnt(2)
	v_perm_b32 v2, v42, v26, s56
	v_perm_b32 v3, v42, v26, s57
	v_perm_b32 v22, v43, v26, s56
	v_perm_b32 v23, v43, v26, s57
	v_fma_mix_f32 v16, v2, v33, v16 op_sel_hi:[1,0,0]
	v_fma_mix_f32 v17, v2, v33, v17 op_sel:[1,0,0] op_sel_hi:[1,0,0]
	v_fma_mix_f32 v14, v3, v33, v14 op_sel_hi:[1,0,0]
	v_fma_mix_f32 v15, v3, v33, v15 op_sel:[1,0,0] op_sel_hi:[1,0,0]
	v_fma_mix_f32 v12, v22, v33, v12 op_sel_hi:[1,0,0]
	v_fma_mix_f32 v13, v22, v33, v13 op_sel:[1,0,0] op_sel_hi:[1,0,0]
	v_fma_mix_f32 v10, v23, v33, v10 op_sel_hi:[1,0,0]
	v_fma_mix_f32 v11, v23, v33, v11 op_sel:[1,0,0] op_sel_hi:[1,0,0]
	v_add_f32_e32 v27, v27, v33
.Lagg_ac0:
	s_waitcnt vmcnt(0)
	v_perm_b32 v2, v40, v26, s56
	v_perm_b32 v3, v40, v26, s57
	v_perm_b32 v22, v41, v26, s56
	v_perm_b32 v23, v41, v26, s57
	v_fma_mix_f32 v16, v2, v32, v16 op_sel_hi:[1,0,0]
	v_fma_mix_f32 v17, v2, v32, v17 op_sel:[1,0,0] op_sel_hi:[1,0,0]
	v_fma_mix_f32 v14, v3, v32, v14 op_sel_hi:[1,0,0]
	v_fma_mix_f32 v15, v3, v32, v15 op_sel:[1,0,0] op_sel_hi:[1,0,0]
	v_fma_mix_f32 v12, v22, v32, v12 op_sel_hi:[1,0,0]
	v_fma_mix_f32 v13, v22, v32, v13 op_sel:[1,0,0] op_sel_hi:[1,0,0]
	v_fma_mix_f32 v10, v23, v32, v10 op_sel_hi:[1,0,0]
	v_fma_mix_f32 v11, v23, v32, v11 op_sel:[1,0,0] op_sel_hi:[1,0,0]
	v_add_f32_e32 v27, v27, v32
	s_add_u32 s15, s15, 8
	s_cmp_lt_u32 s15, s14
	s_cbranch_scc1 .Lagg_inner
	s_add_u32 s3, s3, 64
	s_cmp_lt_u32 s3, s2
	s_cbranch_scc1 .Lagg_outer
	v_mov_b32_e32 v18, s12
	v_mov_b32_e32 v19, s13
.LBB1_26:
	s_or_b64 exec, exec, s[22:23]
	v_fmamk_f32 v10, v27, 0xc4900000, v10
	v_fmamk_f32 v11, v27, 0xc4900000, v11
	v_fmamk_f32 v12, v27, 0xc4900000, v12
	v_fmamk_f32 v13, v27, 0xc4900000, v13
	v_fmamk_f32 v14, v27, 0xc4900000, v14
	v_fmamk_f32 v15, v27, 0xc4900000, v15
	v_fmamk_f32 v16, v27, 0xc4900000, v16
	v_fmamk_f32 v17, v27, 0xc4900000, v17
	s_load_dwordx2 s[8:9], s[0:1], 0x40
	s_load_dwordx2 s[10:11], s[0:1], 0x8
	s_load_dwordx4 s[4:7], s[0:1], 0x30
	v_lshlrev_b64 v[44:45], 2, v[8:9]
	v_lshlrev_b32_e32 v42, 10, v1
	v_mov_b32_e32 v43, 0
	s_waitcnt lgkmcnt(0)
	v_max_i32_e32 v25, 1, v25
	v_cvt_f32_u32_e32 v25, v25
	v_div_scale_f32 v46, s[4:5], v25, v25, 1.0
	v_rcp_f32_e32 v52, v46
	v_div_scale_f32 v42, vcc, 1.0, v25, 1.0
	v_fma_f32 v53, -v46, v52, 1.0
	v_fmac_f32_e32 v52, v53, v52
	v_mul_f32_e32 v53, v42, v52
	v_fma_f32 v55, -v46, v53, v42
	v_fmac_f32_e32 v53, v55, v52
	v_fma_f32 v42, -v46, v53, v42
	v_div_fmas_f32 v42, v42, v52, v53
	v_div_fixup_f32 v42, v42, v25, 1.0
	s_waitcnt vmcnt(0)
	v_cvt_f32_f16_e32 v54, v60
	v_cvt_f32_f16_sdwa v55, v60 dst_sel:DWORD dst_unused:UNUSED_PAD src0_sel:WORD_1
	v_cvt_f32_f16_e32 v56, v61
	v_cvt_f32_f16_sdwa v57, v61 dst_sel:DWORD dst_unused:UNUSED_PAD src0_sel:WORD_1
	v_cvt_f32_f16_e32 v58, v62
	v_cvt_f32_f16_sdwa v59, v62 dst_sel:DWORD dst_unused:UNUSED_PAD src0_sel:WORD_1
	v_cvt_f32_f16_e32 v60, v63
	v_cvt_f32_f16_sdwa v61, v63 dst_sel:DWORD dst_unused:UNUSED_PAD src0_sel:WORD_1
	v_lshl_add_u64 v[22:23], s[6:7], 0, v[44:45]
	v_lshl_add_u64 v[44:45], s[8:9], 0, v[44:45]
	v_pk_fma_f32 v[40:41], v[16:17], v[42:43], v[54:55] op_sel_hi:[1,0,1]
	global_load_dwordx4 v[18:21], v[22:23], off
	global_load_dwordx4 v[34:37], v[22:23], off offset:16
	v_pk_fma_f32 v[54:55], v[14:15], v[42:43], v[56:57] op_sel_hi:[1,0,1]
	global_load_dwordx4 v[14:17], v[44:45], off
	v_mov_b32_e32 v22, v40
	v_mov_b32_e32 v23, v41
	global_load_dwordx4 v[38:41], v[44:45], off offset:16
	v_mov_b32_e32 v44, v54
	v_mov_b32_e32 v45, v55
	v_pk_fma_f32 v[12:13], v[12:13], v[42:43], v[58:59] op_sel_hi:[1,0,1]
	v_mov_b32_e32 v25, 0x3b000000
	v_add_f32_e32 v6, 0, v22
	v_add_f32_e32 v6, v6, v23
	v_add_f32_e32 v6, v6, v44
	v_add_f32_e32 v6, v6, v45
	v_mov_b32_e32 v2, v12
	v_mov_b32_e32 v3, v13
	s_nop 0
	v_add_f32_e32 v6, v6, v2
	v_add_f32_e32 v12, v6, v3
	v_pk_fma_f32 v[6:7], v[10:11], v[42:43], v[60:61] op_sel_hi:[1,0,1]
	v_mov_b32_e32 v4, v6
	v_mov_b32_e32 v5, v7
	v_mov_b32_e32 v7, v43
	v_add_f32_e32 v6, v12, v4
	v_add_f32_e32 v6, v6, v5
	s_nop 1
	v_add_f32_dpp v6, v6, v6 quad_perm:[1,0,3,2] row_mask:0xf bank_mask:0xf bound_ctrl:1
	s_nop 1
	v_add_f32_dpp v6, v6, v6 quad_perm:[2,3,0,1] row_mask:0xf bank_mask:0xf bound_ctrl:1
	s_nop 1
	v_add_f32_dpp v6, v6, v6 row_half_mirror row_mask:0xf bank_mask:0xf bound_ctrl:1
	s_nop 1
	v_add_f32_dpp v6, v6, v6 row_mirror row_mask:0xf bank_mask:0xf bound_ctrl:1
	s_nop 1
	v_mov_b32_dpp v7, v6 row_bcast:15 row_mask:0xa bank_mask:0xf
	v_add_f32_e32 v6, v6, v7
	v_mov_b32_e32 v7, v43
	s_nop 1
	v_mov_b32_dpp v7, v6 row_bcast:31 row_mask:0xc bank_mask:0xf
	v_add_f32_e32 v6, v6, v7
	s_nop 0
	v_readlane_b32 s3, v6, 63
	s_nop 1
	v_mul_f32_e32 v6, s3, v25
	v_pk_add_f32 v[8:9], v[22:23], v[6:7] op_sel_hi:[1,0] neg_lo:[0,1] neg_hi:[0,1]
	v_pk_add_f32 v[12:13], v[44:45], v[6:7] op_sel_hi:[1,0] neg_lo:[0,1] neg_hi:[0,1]
	v_pk_mul_f32 v[10:11], v[8:9], v[8:9]
	v_pk_mul_f32 v[22:23], v[12:13], v[12:13]
	v_add_f32_e32 v10, v10, v11
	v_pk_add_f32 v[2:3], v[2:3], v[6:7] op_sel_hi:[1,0] neg_lo:[0,1] neg_hi:[0,1]
	v_add_f32_e32 v10, v10, v22
	v_pk_mul_f32 v[26:27], v[2:3], v[2:3]
	v_add_f32_e32 v10, v10, v23
	v_pk_add_f32 v[4:5], v[4:5], v[6:7] op_sel_hi:[1,0] neg_lo:[0,1] neg_hi:[0,1]
	v_add_f32_e32 v10, v10, v26
	v_pk_mul_f32 v[6:7], v[4:5], v[4:5]
	v_add_f32_e32 v10, v10, v27
	v_add_f32_e32 v6, v10, v6
	v_add_f32_e32 v6, v6, v7
	v_mov_b32_e32 v7, v43
	s_nop 0
	v_add_f32_dpp v6, v6, v6 quad_perm:[1,0,3,2] row_mask:0xf bank_mask:0xf bound_ctrl:1
	s_nop 1
	v_add_f32_dpp v6, v6, v6 quad_perm:[2,3,0,1] row_mask:0xf bank_mask:0xf bound_ctrl:1
	s_nop 1
	v_add_f32_dpp v6, v6, v6 row_half_mirror row_mask:0xf bank_mask:0xf bound_ctrl:1
	s_nop 1
	v_add_f32_dpp v6, v6, v6 row_mirror row_mask:0xf bank_mask:0xf bound_ctrl:1
	s_nop 1
	v_mov_b32_dpp v7, v6 row_bcast:15 row_mask:0xa bank_mask:0xf
	v_add_f32_e32 v6, v6, v7
	s_nop 1
	v_mov_b32_dpp v43, v6 row_bcast:31 row_mask:0xc bank_mask:0xf
	v_add_f32_e32 v6, v6, v43
	s_nop 0
	v_readlane_b32 s3, v6, 63
	v_mov_b32_e32 v6, 0x3727c5ac
	s_nop 0
	v_fmac_f32_e32 v6, s3, v25
	s_mov_b32 s3, 0x800000
	v_mul_f32_e32 v7, 0x4b800000, v6
	v_cmp_gt_f32_e32 vcc, s3, v6
	s_movk_i32 s3, 0x2800
	s_nop 0
	v_cndmask_b32_e32 v6, v6, v7, vcc
	v_rsq_f32_e32 v6, v6
	v_lshrrev_b32_e32 v7, 3, v24
	v_mad_u32_u24 v1, v7, s3, v1
	v_mul_f32_e32 v7, 0x45800000, v6
	v_cndmask_b32_e32 v6, v6, v7, vcc
	v_pk_mul_f32 v[2:3], v[2:3], v[6:7] op_sel_hi:[1,0]
	v_pk_mul_f32 v[10:11], v[12:13], v[6:7] op_sel_hi:[1,0]
	s_waitcnt vmcnt(0)
	v_pk_fma_f32 v[12:13], v[34:35], v[2:3], v[38:39]
	v_pk_mul_f32 v[2:3], v[4:5], v[6:7] op_sel_hi:[1,0]
	v_pk_mul_f32 v[8:9], v[8:9], v[6:7] op_sel_hi:[1,0]
	v_pk_fma_f32 v[6:7], v[36:37], v[2:3], v[40:41]
	v_pk_fma_f32 v[8:9], v[18:19], v[8:9], v[14:15]
	v_cvt_pk_f16_f32 v5, v6, v7
	v_lshlrev_b32_e32 v6, 4, v0
	v_pk_fma_f32 v[10:11], v[20:21], v[10:11], v[16:17]
	v_and_b32_e32 v6, 0x70, v6
	v_cvt_pk_f16_f32 v2, v8, v9
	v_cvt_pk_f16_f32 v3, v10, v11
	v_cvt_pk_f16_f32 v4, v12, v13
	v_lshl_or_b32 v1, v1, 7, v6
	global_store_dwordx4 v1, v[2:5], s[20:21]

LgAq_loop:
	s_waitcnt vmcnt(8) lgkmcnt(0)
	s_barrier
	v_mfma_f32_16x16x32_f16 v[64:67], a[0:3], v[192:195], v[32:35]
	v_mfma_f32_16x16x32_f16 v[68:71], a[4:7], v[192:195], v[36:39]
	v_add_u32_e32 v5, s29, v4
	v_xor_b32_e32 v6, 64, v5
	s_add_u32 s29, s29, 0x4000
	s_cmp_ge_u32 s29, 0x14000
	s_cselect_b32 s29, 0, s29
	v_mfma_f32_16x16x32_f16 v[72:75], a[8:11], v[192:195], v[40:43]
	ds_read_b128 v[128:131], v5 offset:0
	v_mfma_f32_16x16x32_f16 v[76:79], a[12:15], v[192:195], v[44:47]
	ds_read_b128 v[132:135], v6 offset:0
	v_max3_f32 v16, |v48|, 0, |v49|
	v_mfma_f32_16x16x32_f16 v[64:67], a[16:19], v[196:199], v[64:67]
	ds_read_b128 v[136:139], v5 offset:2048
	v_max3_f32 v16, v16, |v50|, |v51|
	v_mfma_f32_16x16x32_f16 v[68:71], a[20:23], v[196:199], v[68:71]
	ds_read_b128 v[140:143], v6 offset:2048
	v_max3_f32 v16, v16, |v52|, |v53|
	v_mfma_f32_16x16x32_f16 v[72:75], a[24:27], v[196:199], v[72:75]
	ds_read_b128 v[144:147], v5 offset:4096
	v_max3_f32 v16, v16, |v54|, |v55|
	v_mfma_f32_16x16x32_f16 v[76:79], a[28:31], v[196:199], v[76:79]
	ds_read_b128 v[148:151], v6 offset:4096
	v_max3_f32 v16, v16, |v56|, |v57|
	v_mfma_f32_16x16x32_f16 v[64:67], a[32:35], v[200:203], v[64:67]
	ds_read_b128 v[152:155], v5 offset:6144
	v_max3_f32 v16, v16, |v58|, |v59|
	v_mfma_f32_16x16x32_f16 v[68:71], a[36:39], v[200:203], v[68:71]
	ds_read_b128 v[156:159], v6 offset:6144
	v_max3_f32 v16, v16, |v60|, |v61|
	v_mfma_f32_16x16x32_f16 v[72:75], a[40:43], v[200:203], v[72:75]
	ds_read_b128 v[160:163], v5 offset:8192
	v_max3_f32 v16, v16, |v62|, |v63|
	v_mfma_f32_16x16x32_f16 v[76:79], a[44:47], v[200:203], v[76:79]
	ds_read_b128 v[164:167], v6 offset:8192
	v_mov_b32_e32 v17, v16
	v_mfma_f32_16x16x32_f16 v[64:67], a[48:51], v[204:207], v[64:67]
	ds_read_b128 v[168:171], v5 offset:10240
	v_mov_b32_e32 v18, v16
	v_mfma_f32_16x16x32_f16 v[68:71], a[52:55], v[204:207], v[68:71]
	ds_read_b128 v[172:175], v6 offset:10240
	v_permlane32_swap_b32_e32 v17, v18
	v_mfma_f32_16x16x32_f16 v[72:75], a[56:59], v[204:207], v[72:75]
	ds_read_b128 v[176:179], v5 offset:12288
	v_max_f32_e32 v16, v17, v18
	v_mfma_f32_16x16x32_f16 v[76:79], a[60:63], v[204:207], v[76:79]
	ds_read_b128 v[180:183], v6 offset:12288
	v_mov_b32_e32 v17, v16
	v_mfma_f32_16x16x32_f16 v[64:67], a[64:67], v[208:211], v[64:67]
	ds_read_b128 v[184:187], v5 offset:14336
	v_mfma_f32_16x16x32_f16 v[68:71], a[68:71], v[208:211], v[68:71]
	ds_read_b128 v[188:191], v6 offset:14336
	v_mov_b32_e32 v18, v16
	v_mfma_f32_16x16x32_f16 v[72:75], a[72:75], v[208:211], v[72:75]
	s_nop 0
	v_permlane16_swap_b32_e32 v17, v18
	v_mfma_f32_16x16x32_f16 v[76:79], a[76:79], v[208:211], v[76:79]
	v_max_f32_e32 v16, v17, v18
	v_mfma_f32_16x16x32_f16 v[64:67], a[80:83], v[212:215], v[64:67]
	v_rcp_f32_e32 v19, v16
	v_mfma_f32_16x16x32_f16 v[68:71], a[84:87], v[212:215], v[68:71]
	v_cmp_lt_f32_e32 vcc, 0, v16
	v_mfma_f32_16x16x32_f16 v[72:75], a[88:91], v[212:215], v[72:75]
	s_mov_b32 m0, s28
	s_add_u32 s28, s28, 0x4000
	s_cmp_ge_u32 s28, s46
	s_cselect_b32 s28, s47, s28
	global_load_lds_dwordx4 v9, s[26:27]
	v_mul_f32_e32 v19, 0x42fe0000, v19
	v_mfma_f32_16x16x32_f16 v[76:79], a[92:95], v[212:215], v[76:79]
	v_mul_f32_e32 v20, 0x3c010204, v16
	v_mfma_f32_16x16x32_f16 v[64:67], a[96:99], v[216:219], v[64:67]
	v_cndmask_b32_e32 v19, 0, v19, vcc
	v_mfma_f32_16x16x32_f16 v[68:71], a[100:103], v[216:219], v[68:71]
	v_cndmask_b32_e32 v20, 1.0, v20, vcc
	v_mfma_f32_16x16x32_f16 v[72:75], a[104:107], v[216:219], v[72:75]
	v_fmaak_f32 v96, v19, v48, 0x4b400080
	v_mfma_f32_16x16x32_f16 v[76:79], a[108:111], v[216:219], v[76:79]
	v_fmaak_f32 v97, v19, v49, 0x4b400080
	v_mfma_f32_16x16x32_f16 v[64:67], a[112:115], v[220:223], v[64:67]
	v_fmaak_f32 v98, v19, v50, 0x4b400080
	v_mfma_f32_16x16x32_f16 v[68:71], a[116:119], v[220:223], v[68:71]
	v_fmaak_f32 v99, v19, v51, 0x4b400080
	v_mfma_f32_16x16x32_f16 v[72:75], a[120:123], v[220:223], v[72:75]
	v_mfma_f32_16x16x32_f16 v[76:79], a[124:127], v[220:223], v[76:79]
	v_fmaak_f32 v100, v19, v52, 0x4b400080
	v_mfma_f32_16x16x32_f16 v[64:67], a[128:131], v[224:227], v[64:67]
	v_fmaak_f32 v101, v19, v53, 0x4b400080
	v_mfma_f32_16x16x32_f16 v[68:71], a[132:135], v[224:227], v[68:71]
	global_load_lds_dwordx4 v9, s[26:27] offset:1024
	v_fmaak_f32 v102, v19, v54, 0x4b400080
	v_mfma_f32_16x16x32_f16 v[72:75], a[136:139], v[224:227], v[72:75]
	v_fmaak_f32 v103, v19, v55, 0x4b400080
	v_mfma_f32_16x16x32_f16 v[76:79], a[140:143], v[224:227], v[76:79]
	v_fmaak_f32 v104, v19, v56, 0x4b400080
	v_mfma_f32_16x16x32_f16 v[64:67], a[144:147], v[228:231], v[64:67]
	v_fmaak_f32 v105, v19, v57, 0x4b400080
	v_mfma_f32_16x16x32_f16 v[68:71], a[148:151], v[228:231], v[68:71]
	v_fmaak_f32 v106, v19, v58, 0x4b400080
	v_mfma_f32_16x16x32_f16 v[72:75], a[152:155], v[228:231], v[72:75]
	v_fmaak_f32 v107, v19, v59, 0x4b400080
	v_mfma_f32_16x16x32_f16 v[76:79], a[156:159], v[228:231], v[76:79]
	v_fmaak_f32 v108, v19, v60, 0x4b400080
	v_mfma_f32_16x16x32_f16 v[64:67], a[160:163], v[232:235], v[64:67]
	v_fmaak_f32 v109, v19, v61, 0x4b400080
	v_mfma_f32_16x16x32_f16 v[68:71], a[164:167], v[232:235], v[68:71]
	v_fmaak_f32 v110, v19, v62, 0x4b400080
	v_mfma_f32_16x16x32_f16 v[72:75], a[168:171], v[232:235], v[72:75]
	v_fmaak_f32 v111, v19, v63, 0x4b400080
	v_mfma_f32_16x16x32_f16 v[76:79], a[172:175], v[232:235], v[76:79]
	v_perm_b32 v21, v97, v96, s44
	v_mfma_f32_16x16x32_f16 v[64:67], a[176:179], v[236:239], v[64:67]
	s_add_u32 m0, m0, 0x800
	s_nop 0
	global_load_lds_dwordx4 v10, s[26:27]
	v_mfma_f32_16x16x32_f16 v[68:71], a[180:183], v[236:239], v[68:71]
	v_perm_b32 v22, v99, v98, s44
	v_mfma_f32_16x16x32_f16 v[72:75], a[184:187], v[236:239], v[72:75]
	v_perm_b32 v23, v101, v100, s44
	v_mfma_f32_16x16x32_f16 v[76:79], a[188:191], v[236:239], v[76:79]
	v_perm_b32 v24, v103, v102, s44
	v_mfma_f32_16x16x32_f16 v[64:67], a[192:195], v[240:243], v[64:67]
	v_perm_b32 v25, v105, v104, s44
	v_mfma_f32_16x16x32_f16 v[68:71], a[196:199], v[240:243], v[68:71]
	v_perm_b32 v26, v107, v106, s44
	v_mfma_f32_16x16x32_f16 v[72:75], a[200:203], v[240:243], v[72:75]
	v_perm_b32 v27, v109, v108, s44
	v_mfma_f32_16x16x32_f16 v[76:79], a[204:207], v[240:243], v[76:79]
	v_perm_b32 v28, v111, v110, s44
	v_mfma_f32_16x16x32_f16 v[64:67], a[208:211], v[244:247], v[64:67]
	v_perm_b32 v96, v22, v21, s45
	v_mfma_f32_16x16x32_f16 v[68:71], a[212:215], v[244:247], v[68:71]
	v_perm_b32 v97, v24, v23, s45
	v_mfma_f32_16x16x32_f16 v[72:75], a[216:219], v[244:247], v[72:75]
	v_perm_b32 v98, v26, v25, s45
	v_mfma_f32_16x16x32_f16 v[76:79], a[220:223], v[244:247], v[76:79]
	v_perm_b32 v99, v28, v27, s45
	v_mfma_f32_16x16x32_f16 v[64:67], a[224:227], v[248:251], v[64:67]
	global_load_lds_dwordx4 v10, s[26:27] offset:1024
	global_store_dwordx4 v14, v[96:99], s[30:31]
	v_mfma_f32_16x16x32_f16 v[68:71], a[228:231], v[248:251], v[68:71]
	s_add_u32 s26, s26, 0x800
	s_addc_u32 s27, s27, 0
	global_store_dword v112, v20, s[30:31]
	v_mfma_f32_16x16x32_f16 v[72:75], a[232:235], v[248:251], v[72:75]
	v_mfma_f32_16x16x32_f16 v[76:79], a[236:239], v[248:251], v[76:79]
	s_add_u32 s30, s30, 0x8800
	s_addc_u32 s31, s31, 0
	v_mfma_f32_16x16x32_f16 v[64:67], a[240:243], v[252:255], v[64:67]
	v_mfma_f32_16x16x32_f16 v[68:71], a[244:247], v[252:255], v[68:71]
	v_mfma_f32_16x16x32_f16 v[72:75], a[248:251], v[252:255], v[72:75]
	v_mfma_f32_16x16x32_f16 v[76:79], a[252:255], v[252:255], v[76:79]
	s_sub_u32 s24, s24, 1
	s_cmp_le_u32 s24, 1
	s_cbranch_scc1 LgAq_exitA
	s_waitcnt vmcnt(8) lgkmcnt(0)
	s_barrier
	v_mfma_f32_16x16x32_f16 v[48:51], a[0:3], v[128:131], v[32:35]
	v_mfma_f32_16x16x32_f16 v[52:55], a[4:7], v[128:131], v[36:39]
	v_add_u32_e32 v7, s29, v4
	v_xor_b32_e32 v8, 64, v7
	s_add_u32 s29, s29, 0x4000
	s_cmp_ge_u32 s29, 0x14000
	s_cselect_b32 s29, 0, s29
	v_mfma_f32_16x16x32_f16 v[56:59], a[8:11], v[128:131], v[40:43]
	ds_read_b128 v[192:195], v7 offset:0
	v_mfma_f32_16x16x32_f16 v[60:63], a[12:15], v[128:131], v[44:47]
	ds_read_b128 v[196:199], v8 offset:0
	v_max3_f32 v16, |v64|, 0, |v65|
	v_mfma_f32_16x16x32_f16 v[48:51], a[16:19], v[132:135], v[48:51]
	ds_read_b128 v[200:203], v7 offset:2048
	v_max3_f32 v16, v16, |v66|, |v67|
	v_mfma_f32_16x16x32_f16 v[52:55], a[20:23], v[132:135], v[52:55]
	ds_read_b128 v[204:207], v8 offset:2048
	v_max3_f32 v16, v16, |v68|, |v69|
	v_mfma_f32_16x16x32_f16 v[56:59], a[24:27], v[132:135], v[56:59]
	ds_read_b128 v[208:211], v7 offset:4096
	v_max3_f32 v16, v16, |v70|, |v71|
	v_mfma_f32_16x16x32_f16 v[60:63], a[28:31], v[132:135], v[60:63]
	ds_read_b128 v[212:215], v8 offset:4096
	v_max3_f32 v16, v16, |v72|, |v73|
	v_mfma_f32_16x16x32_f16 v[48:51], a[32:35], v[136:139], v[48:51]
	ds_read_b128 v[216:219], v7 offset:6144
	v_max3_f32 v16, v16, |v74|, |v75|
	v_mfma_f32_16x16x32_f16 v[52:55], a[36:39], v[136:139], v[52:55]
	ds_read_b128 v[220:223], v8 offset:6144
	v_max3_f32 v16, v16, |v76|, |v77|
	v_mfma_f32_16x16x32_f16 v[56:59], a[40:43], v[136:139], v[56:59]
	ds_read_b128 v[224:227], v7 offset:8192
	v_max3_f32 v16, v16, |v78|, |v79|
	v_mfma_f32_16x16x32_f16 v[60:63], a[44:47], v[136:139], v[60:63]
	ds_read_b128 v[228:231], v8 offset:8192
	v_mov_b32_e32 v17, v16
	v_mfma_f32_16x16x32_f16 v[48:51], a[48:51], v[140:143], v[48:51]
	ds_read_b128 v[232:235], v7 offset:10240
	v_mov_b32_e32 v18, v16
	v_mfma_f32_16x16x32_f16 v[52:55], a[52:55], v[140:143], v[52:55]
	ds_read_b128 v[236:239], v8 offset:10240
	v_permlane32_swap_b32_e32 v17, v18
	v_mfma_f32_16x16x32_f16 v[56:59], a[56:59], v[140:143], v[56:59]
	ds_read_b128 v[240:243], v7 offset:12288
	v_max_f32_e32 v16, v17, v18
	v_mfma_f32_16x16x32_f16 v[60:63], a[60:63], v[140:143], v[60:63]
	ds_read_b128 v[244:247], v8 offset:12288
	v_mov_b32_e32 v17, v16
	v_mfma_f32_16x16x32_f16 v[48:51], a[64:67], v[144:147], v[48:51]
	ds_read_b128 v[248:251], v7 offset:14336
	v_mfma_f32_16x16x32_f16 v[52:55], a[68:71], v[144:147], v[52:55]
	ds_read_b128 v[252:255], v8 offset:14336
	v_mov_b32_e32 v18, v16
	v_mfma_f32_16x16x32_f16 v[56:59], a[72:75], v[144:147], v[56:59]
	s_nop 0
	v_permlane16_swap_b32_e32 v17, v18
	v_mfma_f32_16x16x32_f16 v[60:63], a[76:79], v[144:147], v[60:63]
	v_max_f32_e32 v16, v17, v18
	v_mfma_f32_16x16x32_f16 v[48:51], a[80:83], v[148:151], v[48:51]
	v_rcp_f32_e32 v19, v16
	v_mfma_f32_16x16x32_f16 v[52:55], a[84:87], v[148:151], v[52:55]
	v_cmp_lt_f32_e32 vcc, 0, v16
	v_mfma_f32_16x16x32_f16 v[56:59], a[88:91], v[148:151], v[56:59]
	s_mov_b32 m0, s28
	s_add_u32 s28, s28, 0x4000
	s_cmp_ge_u32 s28, s46
	s_cselect_b32 s28, s47, s28
	global_load_lds_dwordx4 v9, s[26:27]
	v_mul_f32_e32 v19, 0x42fe0000, v19
	v_mfma_f32_16x16x32_f16 v[60:63], a[92:95], v[148:151], v[60:63]
	v_mul_f32_e32 v20, 0x3c010204, v16
	v_mfma_f32_16x16x32_f16 v[48:51], a[96:99], v[152:155], v[48:51]
	v_cndmask_b32_e32 v19, 0, v19, vcc
	v_mfma_f32_16x16x32_f16 v[52:55], a[100:103], v[152:155], v[52:55]
	v_cndmask_b32_e32 v20, 1.0, v20, vcc
	v_mfma_f32_16x16x32_f16 v[56:59], a[104:107], v[152:155], v[56:59]
	v_fmaak_f32 v96, v19, v64, 0x4b400080
	v_mfma_f32_16x16x32_f16 v[60:63], a[108:111], v[152:155], v[60:63]
	v_fmaak_f32 v97, v19, v65, 0x4b400080
	v_mfma_f32_16x16x32_f16 v[48:51], a[112:115], v[156:159], v[48:51]
	v_fmaak_f32 v98, v19, v66, 0x4b400080
	v_mfma_f32_16x16x32_f16 v[52:55], a[116:119], v[156:159], v[52:55]
	v_fmaak_f32 v99, v19, v67, 0x4b400080
	v_mfma_f32_16x16x32_f16 v[56:59], a[120:123], v[156:159], v[56:59]
	v_mfma_f32_16x16x32_f16 v[60:63], a[124:127], v[156:159], v[60:63]
	v_fmaak_f32 v100, v19, v68, 0x4b400080
	v_mfma_f32_16x16x32_f16 v[48:51], a[128:131], v[160:163], v[48:51]
	v_fmaak_f32 v101, v19, v69, 0x4b400080
	v_mfma_f32_16x16x32_f16 v[52:55], a[132:135], v[160:163], v[52:55]
	global_load_lds_dwordx4 v9, s[26:27] offset:1024
	v_fmaak_f32 v102, v19, v70, 0x4b400080
	v_mfma_f32_16x16x32_f16 v[56:59], a[136:139], v[160:163], v[56:59]
	v_fmaak_f32 v103, v19, v71, 0x4b400080
	v_mfma_f32_16x16x32_f16 v[60:63], a[140:143], v[160:163], v[60:63]
	v_fmaak_f32 v104, v19, v72, 0x4b400080
	v_mfma_f32_16x16x32_f16 v[48:51], a[144:147], v[164:167], v[48:51]
	v_fmaak_f32 v105, v19, v73, 0x4b400080
	v_mfma_f32_16x16x32_f16 v[52:55], a[148:151], v[164:167], v[52:55]
	v_fmaak_f32 v106, v19, v74, 0x4b400080
	v_mfma_f32_16x16x32_f16 v[56:59], a[152:155], v[164:167], v[56:59]
	v_fmaak_f32 v107, v19, v75, 0x4b400080
	v_mfma_f32_16x16x32_f16 v[60:63], a[156:159], v[164:167], v[60:63]
	v_fmaak_f32 v108, v19, v76, 0x4b400080
	v_mfma_f32_16x16x32_f16 v[48:51], a[160:163], v[168:171], v[48:51]
	v_fmaak_f32 v109, v19, v77, 0x4b400080
	v_mfma_f32_16x16x32_f16 v[52:55], a[164:167], v[168:171], v[52:55]
	v_fmaak_f32 v110, v19, v78, 0x4b400080
	v_mfma_f32_16x16x32_f16 v[56:59], a[168:171], v[168:171], v[56:59]
	v_fmaak_f32 v111, v19, v79, 0x4b400080
	v_mfma_f32_16x16x32_f16 v[60:63], a[172:175], v[168:171], v[60:63]
	v_perm_b32 v21, v97, v96, s44
	v_mfma_f32_16x16x32_f16 v[48:51], a[176:179], v[172:175], v[48:51]
	s_add_u32 m0, m0, 0x800
	s_nop 0
	global_load_lds_dwordx4 v10, s[26:27]
	v_mfma_f32_16x16x32_f16 v[52:55], a[180:183], v[172:175], v[52:55]
	v_perm_b32 v22, v99, v98, s44
	v_mfma_f32_16x16x32_f16 v[56:59], a[184:187], v[172:175], v[56:59]
	v_perm_b32 v23, v101, v100, s44
	v_mfma_f32_16x16x32_f16 v[60:63], a[188:191], v[172:175], v[60:63]
	v_perm_b32 v24, v103, v102, s44
	v_mfma_f32_16x16x32_f16 v[48:51], a[192:195], v[176:179], v[48:51]
	v_perm_b32 v25, v105, v104, s44
	v_mfma_f32_16x16x32_f16 v[52:55], a[196:199], v[176:179], v[52:55]
	v_perm_b32 v26, v107, v106, s44
	v_mfma_f32_16x16x32_f16 v[56:59], a[200:203], v[176:179], v[56:59]
	v_perm_b32 v27, v109, v108, s44
	v_mfma_f32_16x16x32_f16 v[60:63], a[204:207], v[176:179], v[60:63]
	v_perm_b32 v28, v111, v110, s44
	v_mfma_f32_16x16x32_f16 v[48:51], a[208:211], v[180:183], v[48:51]
	v_perm_b32 v96, v22, v21, s45
	v_mfma_f32_16x16x32_f16 v[52:55], a[212:215], v[180:183], v[52:55]
	v_perm_b32 v97, v24, v23, s45
	v_mfma_f32_16x16x32_f16 v[56:59], a[216:219], v[180:183], v[56:59]
	v_perm_b32 v98, v26, v25, s45
	v_mfma_f32_16x16x32_f16 v[60:63], a[220:223], v[180:183], v[60:63]
	v_perm_b32 v99, v28, v27, s45
	v_mfma_f32_16x16x32_f16 v[48:51], a[224:227], v[184:187], v[48:51]
	global_load_lds_dwordx4 v10, s[26:27] offset:1024
	global_store_dwordx4 v14, v[96:99], s[30:31]
	v_mfma_f32_16x16x32_f16 v[52:55], a[228:231], v[184:187], v[52:55]
	s_add_u32 s26, s26, 0x800
	s_addc_u32 s27, s27, 0
	global_store_dword v112, v20, s[30:31]
	v_mfma_f32_16x16x32_f16 v[56:59], a[232:235], v[184:187], v[56:59]
	v_mfma_f32_16x16x32_f16 v[60:63], a[236:239], v[184:187], v[60:63]
	s_add_u32 s30, s30, 0x8800
	s_addc_u32 s31, s31, 0
	v_mfma_f32_16x16x32_f16 v[48:51], a[240:243], v[188:191], v[48:51]
	v_mfma_f32_16x16x32_f16 v[52:55], a[244:247], v[188:191], v[52:55]
	v_mfma_f32_16x16x32_f16 v[56:59], a[248:251], v[188:191], v[56:59]
	v_mfma_f32_16x16x32_f16 v[60:63], a[252:255], v[188:191], v[60:63]
	s_sub_u32 s24, s24, 1
	s_cmp_le_u32 s24, 1
	s_cbranch_scc0 LgAq_loop
	s_nop 7
	s_nop 7
	v_max3_f32 v16, |v48|, 0, |v49|
	v_max3_f32 v16, v16, |v50|, |v51|
	v_max3_f32 v16, v16, |v52|, |v53|
	v_max3_f32 v16, v16, |v54|, |v55|
	v_max3_f32 v16, v16, |v56|, |v57|
	v_max3_f32 v16, v16, |v58|, |v59|
	v_max3_f32 v16, v16, |v60|, |v61|
	v_max3_f32 v16, v16, |v62|, |v63|
	v_mov_b32_e32 v17, v16
	v_mov_b32_e32 v18, v16
	s_nop 1
	v_permlane32_swap_b32_e32 v17, v18
	v_max_f32_e32 v16, v17, v18
	v_mov_b32_e32 v17, v16
	v_mov_b32_e32 v18, v16
	s_nop 1
	v_permlane16_swap_b32_e32 v17, v18
	v_max_f32_e32 v16, v17, v18
	v_rcp_f32_e32 v19, v16
	v_cmp_lt_f32_e32 vcc, 0, v16
	v_mul_f32_e32 v19, 0x42fe0000, v19
	v_mul_f32_e32 v20, 0x3c010204, v16
	v_cndmask_b32_e32 v19, 0, v19, vcc
	v_cndmask_b32_e32 v20, 1.0, v20, vcc
	v_fmaak_f32 v96, v19, v48, 0x4b400080
	v_fmaak_f32 v97, v19, v49, 0x4b400080
	v_fmaak_f32 v98, v19, v50, 0x4b400080
	v_fmaak_f32 v99, v19, v51, 0x4b400080
	v_fmaak_f32 v100, v19, v52, 0x4b400080
	v_fmaak_f32 v101, v19, v53, 0x4b400080
	v_fmaak_f32 v102, v19, v54, 0x4b400080
	v_fmaak_f32 v103, v19, v55, 0x4b400080
	v_fmaak_f32 v104, v19, v56, 0x4b400080
	v_fmaak_f32 v105, v19, v57, 0x4b400080
	v_fmaak_f32 v106, v19, v58, 0x4b400080
	v_fmaak_f32 v107, v19, v59, 0x4b400080
	v_fmaak_f32 v108, v19, v60, 0x4b400080
	v_fmaak_f32 v109, v19, v61, 0x4b400080
	v_fmaak_f32 v110, v19, v62, 0x4b400080
	v_fmaak_f32 v111, v19, v63, 0x4b400080
	v_perm_b32 v21, v97, v96, s44
	v_perm_b32 v22, v99, v98, s44
	v_perm_b32 v23, v101, v100, s44
	v_perm_b32 v24, v103, v102, s44
	v_perm_b32 v25, v105, v104, s44
	v_perm_b32 v26, v107, v106, s44
	v_perm_b32 v27, v109, v108, s44
	v_perm_b32 v28, v111, v110, s44
	v_perm_b32 v96, v22, v21, s45
	v_perm_b32 v97, v24, v23, s45
	v_perm_b32 v98, v26, v25, s45
	v_perm_b32 v99, v28, v27, s45
	global_store_dwordx4 v14, v[96:99], s[30:31]
	global_store_dword v112, v20, s[30:31]
	s_add_u32 s30, s30, 0x8800
	s_addc_u32 s31, s31, 0
	s_endpgm
LgAq_exitA:
	s_nop 7
	s_nop 7
	v_max3_f32 v16, |v64|, 0, |v65|
	v_max3_f32 v16, v16, |v66|, |v67|
	v_max3_f32 v16, v16, |v68|, |v69|
	v_max3_f32 v16, v16, |v70|, |v71|
	v_max3_f32 v16, v16, |v72|, |v73|
	v_max3_f32 v16, v16, |v74|, |v75|
	v_max3_f32 v16, v16, |v76|, |v77|
	v_max3_f32 v16, v16, |v78|, |v79|
	v_mov_b32_e32 v17, v16
	v_mov_b32_e32 v18, v16
	s_nop 1
	v_permlane32_swap_b32_e32 v17, v18
	v_max_f32_e32 v16, v17, v18
	v_mov_b32_e32 v17, v16
	v_mov_b32_e32 v18, v16
	s_nop 1
	v_permlane16_swap_b32_e32 v17, v18
	v_max_f32_e32 v16, v17, v18
	v_rcp_f32_e32 v19, v16
	v_cmp_lt_f32_e32 vcc, 0, v16
	v_mul_f32_e32 v19, 0x42fe0000, v19
	v_mul_f32_e32 v20, 0x3c010204, v16
	v_cndmask_b32_e32 v19, 0, v19, vcc
	v_cndmask_b32_e32 v20, 1.0, v20, vcc
	v_fmaak_f32 v96, v19, v64, 0x4b400080
	v_fmaak_f32 v97, v19, v65, 0x4b400080
	v_fmaak_f32 v98, v19, v66, 0x4b400080
	v_fmaak_f32 v99, v19, v67, 0x4b400080
	v_fmaak_f32 v100, v19, v68, 0x4b400080
	v_fmaak_f32 v101, v19, v69, 0x4b400080
	v_fmaak_f32 v102, v19, v70, 0x4b400080
	v_fmaak_f32 v103, v19, v71, 0x4b400080
	v_fmaak_f32 v104, v19, v72, 0x4b400080
	v_fmaak_f32 v105, v19, v73, 0x4b400080
	v_fmaak_f32 v106, v19, v74, 0x4b400080
	v_fmaak_f32 v107, v19, v75, 0x4b400080
	v_fmaak_f32 v108, v19, v76, 0x4b400080
	v_fmaak_f32 v109, v19, v77, 0x4b400080
	v_fmaak_f32 v110, v19, v78, 0x4b400080
	v_fmaak_f32 v111, v19, v79, 0x4b400080
	v_perm_b32 v21, v97, v96, s44
	v_perm_b32 v22, v99, v98, s44
	v_perm_b32 v23, v101, v100, s44
	v_perm_b32 v24, v103, v102, s44
	v_perm_b32 v25, v105, v104, s44
	v_perm_b32 v26, v107, v106, s44
	v_perm_b32 v27, v109, v108, s44
	v_perm_b32 v28, v111, v110, s44
	v_perm_b32 v96, v22, v21, s45
	v_perm_b32 v97, v24, v23, s45
	v_perm_b32 v98, v26, v25, s45
	v_perm_b32 v99, v28, v27, s45
	global_store_dwordx4 v14, v[96:99], s[30:31]
	global_store_dword v112, v20, s[30:31]
	s_add_u32 s30, s30, 0x8800
	s_addc_u32 s31, s31, 0
	s_endpgm
